# merged item loop: next-item prefetch address corrected for round 3
# speedup vs baseline: 1.0106x; 1.0029x over previous
; __device__ __forceinline__ void gdn_local_item(const Params& P, LAS unsigned char* lds, int item, int tid, bool defer, int& pend, unsigned& pend_fb) {
;     ...
;         for (int r = 0; r < 7; ++r) {
;             const int id = tid + 512 * r;
;             const int row = id / 48, rem = id - row * 48, part = rem >> 4, ck = rem & 15, s = n * 64 + row - 3;
;             pr[r] = (v4u){0u, 0u, 0u, 0u};
;             if (id < 67 * 48 && s >= 0) pr[r] = *(const v4u*)(QKV + (size_t)(b * SEQ + s) * 1536 + part * 512 + h * 128 + ck * 8);
; __global__ void __launch_bounds__(NWAVES * 64, 2) hybrid_fwd(Params P) {
;     ...
;               if (NWK == 224) {
;                   for (int r = 0; r < 3; ++r) { const int q = 224 * r + wk; gdn_local_item(P, lds, (q & 7) * 128 + (q >> 3), tid, r > 0, pend, pend_fb); }
;                   if (wk < 192) { const int q = 672 + wk; gdn_local_item(P, lds, (q & 7) * 128 + (q >> 3), tid, true, pend, pend_fb); }
;                   if (wk < 160) { const int q = 864 + wk; gdn_local_item(P, lds, (q & 7) * 128 + (q >> 3), tid, true, pend, pend_fb); }
.LBB0_517:
	v_ashrrev_i32_e32 v92, 3, v91
	v_and_b32_e32 v46, 7, v91
	s_movk_i32 s0, 0x300
	v_lshlrev_b32_e32 v51, 6, v46
	v_lshlrev_b32_e32 v52, 5, v46
	s_waitcnt vmcnt(0)
	s_mul_i32 s98, s58, 0xe0
	v_readlane_b32 s99, v255, 10
	s_add_i32 s98, s98, s99
	s_addk_i32 s98, 0xe0
	s_cmp_eq_u32 s58, 3
	s_cselect_b32 s99, 32, 0
	s_sub_i32 s98, s98, s99
	s_lshr_b32 s99, s98, 3
	s_cmpk_gt_u32 s99, 0x7f
	s_cbranch_scc1 .Lpf_skipA
	s_and_b32 s98, s98, 7
	s_lshr_b32 s100, s98, 2
	s_and_b32 s98, s98, 3
	s_lshl_b32 s100, s100, 13
	s_lshl_b32 s99, s99, 6
	s_add_i32 s99, s99, s100
	s_add_i32 s99, s99, -3
	s_mul_i32 s99, s99, 0xc00
	s_lshl_b32 s98, s98, 8
	s_add_u32 s98, s99, s98
	s_add_u32 s100, s24, 0x3c00000
	s_addc_u32 s101, s25, 0
	s_add_u32 s100, s100, s98
	s_addc_u32 s101, s101, 0
	s_mov_b32 s98, 0x2aaaaaab
	v_mul_hi_u32 v250, v0, s98
	v_mul_u32_u24_e32 v251, 6, v250
	v_sub_u32_e32 v251, v0, v251
	v_lshrrev_b32_e32 v252, 1, v251
	v_and_b32_e32 v251, 1, v251
	v_mul_u32_u24_e32 v250, 0xc00, v250
	v_lshl_add_u32 v250, v252, 10, v250
	v_lshl_add_u32 v250, v251, 7, v250
	v_mov_b32_e32 v251, 0x192
	v_cmp_gt_u32_e64 s[98:99], v251, v0
	s_mov_b64 exec, s[98:99]
	global_load_dword v253, v250, s[100:101]
	s_mov_b64 exec, -1
